# cmp-attn importance head sums: remaining mov0+mov_dpp+pk_add groups fused into v_add_f32_dpp (bit-identical, ~10 VALU slots fewer per pass-2 quad-tile)
# baseline (speedup 1.0000x reference)
; __device__ __forceinline__ float dpp_xor1(float v) { return __int_as_float(__builtin_amdgcn_update_dpp(0, __float_as_int(v), 0xB1, 0xf, 0xf, false)); }
; __device__ __forceinline__ float dpp_xor2(float v) { return __int_as_float(__builtin_amdgcn_update_dpp(0, __float_as_int(v), 0x4E, 0xf, 0xf, false)); }
;     ...
;                         if (MODE == 2 && pass == 1) {
;                             float base[4], im3[4], rot[4];
; #pragma unroll
;                             for (int kt = 0; kt < 4; ++kt) { float im[4];
; #pragma unroll
;                                 for (int r = 0; r < 4; ++r) { float v = p[kt][r]; v += dpp_xor1(v); v += dpp_xor2(v); im[r] = v; }
;                                 base[kt] = 2.0f * (im[0] + im[1] + im[2]) + im[3]; im3[kt] = im[3]; }
; #pragma unroll
;                             for (int kt = 0; kt < 4; ++kt) rot[kt] = __shfl(im3[kt], (lane + 48) & 63);
; #pragma unroll
;                             for (int kt = 0; kt < 4; ++kt) { const float pv3 = q > 0 ? rot[kt] : (kt == 0 ? carry3[qd] : rot[kt > 0 ? kt - 1 : 0]);
;                                 const int jg = (p0 + 16 * kt + 4 * q) >> 2;
;                                 if (hr == 0 && jg < 256) sscore[(tq - t0) * SSTR + jg] = base[kt] + pv3; }
.LBB0_892:
	v_add_u32_e32 v126, s27, v141
	v_ashrrev_i32_e32 v127, 2, v126
	s_and_b64 vcc, exec, s[36:37]
	v_cmp_gt_i32_e64 s[14:15], s23, v127
	s_cbranch_vccnz .LBB0_902
	v_add_f32_dpp v128, v217, v217 quad_perm:[1,0,3,2] row_mask:0xf bank_mask:0xf bound_ctrl:1
	v_add_f32_dpp v122, v150, v150 quad_perm:[1,0,3,2] row_mask:0xf bank_mask:0xf bound_ctrl:1
	v_add_f32_dpp v123, v151, v151 quad_perm:[1,0,3,2] row_mask:0xf bank_mask:0xf bound_ctrl:1
	v_add_f32_dpp v243, v128, v128 quad_perm:[2,3,0,1] row_mask:0xf bank_mask:0xf bound_ctrl:1
	v_add_f32_dpp v128, v221, v221 quad_perm:[1,0,3,2] row_mask:0xf bank_mask:0xf bound_ctrl:1
	v_add_f32_dpp v249, v216, v216 quad_perm:[1,0,3,2] row_mask:0xf bank_mask:0xf bound_ctrl:1
	v_add_f32_dpp v124, v122, v122 quad_perm:[2,3,0,1] row_mask:0xf bank_mask:0xf bound_ctrl:1
	v_add_f32_dpp v241, v128, v128 quad_perm:[2,3,0,1] row_mask:0xf bank_mask:0xf bound_ctrl:1
	v_add_f32_dpp v128, v225, v225 quad_perm:[1,0,3,2] row_mask:0xf bank_mask:0xf bound_ctrl:1
	v_add_f32_dpp v125, v123, v123 quad_perm:[2,3,0,1] row_mask:0xf bank_mask:0xf bound_ctrl:1
	v_add_f32_dpp v250, v249, v249 quad_perm:[2,3,0,1] row_mask:0xf bank_mask:0xf bound_ctrl:1
	v_add_f32_dpp v164, v128, v128 quad_perm:[2,3,0,1] row_mask:0xf bank_mask:0xf bound_ctrl:1
	v_add_f32_dpp v128, v229, v229 quad_perm:[1,0,3,2] row_mask:0xf bank_mask:0xf bound_ctrl:1
	v_add_f32_dpp v238, v218, v218 quad_perm:[1,0,3,2] row_mask:0xf bank_mask:0xf bound_ctrl:1
	v_add_f32_dpp v240, v219, v219 quad_perm:[1,0,3,2] row_mask:0xf bank_mask:0xf bound_ctrl:1
	v_add_f32_dpp v132, v128, v128 quad_perm:[2,3,0,1] row_mask:0xf bank_mask:0xf bound_ctrl:1
	v_and_or_b32 v128, v244, 64, v139
	v_lshlrev_b32_e32 v128, 2, v128
	ds_bpermute_b32 v192, v128, v243
	ds_bpermute_b32 v248, v128, v241
	ds_bpermute_b32 v134, v128, v164
	ds_bpermute_b32 v128, v128, v132
	v_add_f32_dpp v246, v220, v220 quad_perm:[1,0,3,2] row_mask:0xf bank_mask:0xf bound_ctrl:1
	v_add_f32_dpp v135, v222, v222 quad_perm:[1,0,3,2] row_mask:0xf bank_mask:0xf bound_ctrl:1
	v_add_f32_dpp v137, v223, v223 quad_perm:[1,0,3,2] row_mask:0xf bank_mask:0xf bound_ctrl:1
	v_add_f32_dpp v235, v224, v224 quad_perm:[1,0,3,2] row_mask:0xf bank_mask:0xf bound_ctrl:1
	v_add_f32_dpp v129, v226, v226 quad_perm:[1,0,3,2] row_mask:0xf bank_mask:0xf bound_ctrl:1
	v_add_f32_dpp v131, v227, v227 quad_perm:[1,0,3,2] row_mask:0xf bank_mask:0xf bound_ctrl:1
	v_add_f32_dpp v191, v228, v228 quad_perm:[1,0,3,2] row_mask:0xf bank_mask:0xf bound_ctrl:1
	v_add_f32_dpp v239, v238, v238 quad_perm:[2,3,0,1] row_mask:0xf bank_mask:0xf bound_ctrl:1
	v_add_f32_dpp v245, v240, v240 quad_perm:[2,3,0,1] row_mask:0xf bank_mask:0xf bound_ctrl:1
	v_add_f32_dpp v247, v246, v246 quad_perm:[2,3,0,1] row_mask:0xf bank_mask:0xf bound_ctrl:1
	v_add_f32_dpp v136, v135, v135 quad_perm:[2,3,0,1] row_mask:0xf bank_mask:0xf bound_ctrl:1
	v_add_f32_dpp v165, v137, v137 quad_perm:[2,3,0,1] row_mask:0xf bank_mask:0xf bound_ctrl:1
	v_add_f32_dpp v237, v235, v235 quad_perm:[2,3,0,1] row_mask:0xf bank_mask:0xf bound_ctrl:1
	v_add_f32_dpp v130, v129, v129 quad_perm:[2,3,0,1] row_mask:0xf bank_mask:0xf bound_ctrl:1
	v_add_f32_dpp v133, v131, v131 quad_perm:[2,3,0,1] row_mask:0xf bank_mask:0xf bound_ctrl:1
	v_add_f32_dpp v236, v191, v191 quad_perm:[2,3,0,1] row_mask:0xf bank_mask:0xf bound_ctrl:1
	s_and_b64 s[14:15], s[2:3], s[14:15]
	s_and_saveexec_b64 s[4:5], s[14:15]
	s_cbranch_execz .LBB0_895
	v_add_f32_e32 v122, v124, v250
	v_add_f32_e32 v122, v122, v125
	v_fmac_f32_e32 v243, 2.0, v122
	s_waitcnt lgkmcnt(3)
	v_cndmask_b32_e64 v123, v192, v234, s[0:1]
	v_lshl_add_u32 v122, v127, 2, v231
	v_add_f32_e32 v123, v243, v123
	ds_write_b32 v122, v123 offset:16384

; __device__ __forceinline__ float dpp_xor1(float v) { return __int_as_float(__builtin_amdgcn_update_dpp(0, __float_as_int(v), 0xB1, 0xf, 0xf, false)); }
; __device__ __forceinline__ float dpp_xor2(float v) { return __int_as_float(__builtin_amdgcn_update_dpp(0, __float_as_int(v), 0x4E, 0xf, 0xf, false)); }
;     ...
;                         if (MODE == 2 && pass == 1) {
;                             float base[4], im3[4], rot[4];
; #pragma unroll
;                             for (int kt = 0; kt < 4; ++kt) { float im[4];
; #pragma unroll
;                                 for (int r = 0; r < 4; ++r) { float v = p[kt][r]; v += dpp_xor1(v); v += dpp_xor2(v); im[r] = v; }
;                                 base[kt] = 2.0f * (im[0] + im[1] + im[2]) + im[3]; im3[kt] = im[3]; }
; #pragma unroll
;                             for (int kt = 0; kt < 4; ++kt) rot[kt] = __shfl(im3[kt], (lane + 48) & 63);
; #pragma unroll
;                             for (int kt = 0; kt < 4; ++kt) { const float pv3 = q > 0 ? rot[kt] : (kt == 0 ? carry3[qd] : rot[kt > 0 ? kt - 1 : 0]);
;                                 const int jg = (p0 + 16 * kt + 4 * q) >> 2;
;                                 if (hr == 0 && jg < 256) sscore[(tq - t0) * SSTR + jg] = base[kt] + pv3; }
.LBB0_908:
	s_and_b64 vcc, exec, s[36:37]
	s_cbranch_vccnz .LBB0_918
	v_add_f32_dpp v94, v217, v217 quad_perm:[1,0,3,2] row_mask:0xf bank_mask:0xf bound_ctrl:1
	v_add_f32_dpp v90, v150, v150 quad_perm:[1,0,3,2] row_mask:0xf bank_mask:0xf bound_ctrl:1
	v_add_f32_dpp v91, v151, v151 quad_perm:[1,0,3,2] row_mask:0xf bank_mask:0xf bound_ctrl:1
	v_add_f32_dpp v120, v94, v94 quad_perm:[2,3,0,1] row_mask:0xf bank_mask:0xf bound_ctrl:1
	v_add_f32_dpp v94, v221, v221 quad_perm:[1,0,3,2] row_mask:0xf bank_mask:0xf bound_ctrl:1
	v_add_f32_dpp v118, v216, v216 quad_perm:[1,0,3,2] row_mask:0xf bank_mask:0xf bound_ctrl:1
	v_add_f32_dpp v92, v90, v90 quad_perm:[2,3,0,1] row_mask:0xf bank_mask:0xf bound_ctrl:1
	v_add_f32_dpp v113, v94, v94 quad_perm:[2,3,0,1] row_mask:0xf bank_mask:0xf bound_ctrl:1
	v_add_f32_dpp v94, v225, v225 quad_perm:[1,0,3,2] row_mask:0xf bank_mask:0xf bound_ctrl:1
	v_add_f32_dpp v93, v91, v91 quad_perm:[2,3,0,1] row_mask:0xf bank_mask:0xf bound_ctrl:1
	v_add_f32_dpp v119, v118, v118 quad_perm:[2,3,0,1] row_mask:0xf bank_mask:0xf bound_ctrl:1
	v_add_f32_dpp v105, v94, v94 quad_perm:[2,3,0,1] row_mask:0xf bank_mask:0xf bound_ctrl:1
	v_add_f32_dpp v94, v229, v229 quad_perm:[1,0,3,2] row_mask:0xf bank_mask:0xf bound_ctrl:1
	v_add_f32_dpp v110, v218, v218 quad_perm:[1,0,3,2] row_mask:0xf bank_mask:0xf bound_ctrl:1
	v_add_f32_dpp v112, v219, v219 quad_perm:[1,0,3,2] row_mask:0xf bank_mask:0xf bound_ctrl:1
	v_add_f32_dpp v98, v94, v94 quad_perm:[2,3,0,1] row_mask:0xf bank_mask:0xf bound_ctrl:1
	v_and_or_b32 v94, v244, 64, v139
	v_lshlrev_b32_e32 v94, 2, v94
	ds_bpermute_b32 v121, v94, v120
	ds_bpermute_b32 v117, v94, v113
	ds_bpermute_b32 v101, v94, v105
	ds_bpermute_b32 v94, v94, v98
	v_add_f32_dpp v115, v220, v220 quad_perm:[1,0,3,2] row_mask:0xf bank_mask:0xf bound_ctrl:1
	v_add_f32_dpp v102, v222, v222 quad_perm:[1,0,3,2] row_mask:0xf bank_mask:0xf bound_ctrl:1
	v_add_f32_dpp v104, v223, v223 quad_perm:[1,0,3,2] row_mask:0xf bank_mask:0xf bound_ctrl:1
	v_add_f32_dpp v108, v224, v224 quad_perm:[1,0,3,2] row_mask:0xf bank_mask:0xf bound_ctrl:1
	v_add_f32_dpp v95, v226, v226 quad_perm:[1,0,3,2] row_mask:0xf bank_mask:0xf bound_ctrl:1
	v_add_f32_dpp v97, v227, v227 quad_perm:[1,0,3,2] row_mask:0xf bank_mask:0xf bound_ctrl:1
	v_add_f32_dpp v100, v228, v228 quad_perm:[1,0,3,2] row_mask:0xf bank_mask:0xf bound_ctrl:1
	v_cmp_gt_i32_e32 vcc, s23, v127
	v_add_f32_dpp v111, v110, v110 quad_perm:[2,3,0,1] row_mask:0xf bank_mask:0xf bound_ctrl:1
	v_add_f32_dpp v114, v112, v112 quad_perm:[2,3,0,1] row_mask:0xf bank_mask:0xf bound_ctrl:1
	v_add_f32_dpp v116, v115, v115 quad_perm:[2,3,0,1] row_mask:0xf bank_mask:0xf bound_ctrl:1
	v_add_f32_dpp v103, v102, v102 quad_perm:[2,3,0,1] row_mask:0xf bank_mask:0xf bound_ctrl:1
	v_add_f32_dpp v106, v104, v104 quad_perm:[2,3,0,1] row_mask:0xf bank_mask:0xf bound_ctrl:1
	v_add_f32_dpp v109, v108, v108 quad_perm:[2,3,0,1] row_mask:0xf bank_mask:0xf bound_ctrl:1
	v_add_f32_dpp v96, v95, v95 quad_perm:[2,3,0,1] row_mask:0xf bank_mask:0xf bound_ctrl:1
	v_add_f32_dpp v99, v97, v97 quad_perm:[2,3,0,1] row_mask:0xf bank_mask:0xf bound_ctrl:1
	v_add_f32_dpp v107, v100, v100 quad_perm:[2,3,0,1] row_mask:0xf bank_mask:0xf bound_ctrl:1
	s_and_b64 s[14:15], s[2:3], vcc
	s_and_saveexec_b64 s[4:5], s[14:15]
	s_cbranch_execz .LBB0_911
	v_add_f32_e32 v90, v92, v119
	v_add_f32_e32 v90, v90, v93
	v_fmac_f32_e32 v120, 2.0, v90
	s_waitcnt lgkmcnt(3)
	v_cndmask_b32_e64 v91, v121, v233, s[0:1]
	v_lshl_add_u32 v90, v127, 2, v232
	v_add_f32_e32 v91, v120, v91
	ds_write_b32 v90, v91 offset:16384
